# grid barriers: acquire invalidate issued behind the arrival atomic (overlaps the wait) instead of after the release; on top of previous best
# baseline (speedup 1.0000x reference)
; __device__ __forceinline__ unsigned xb_ld(unsigned* p)              { return __hip_atomic_load(p, __ATOMIC_RELAXED, __HIP_MEMORY_SCOPE_AGENT); }
; __device__ __forceinline__ unsigned xb_add(unsigned* p, unsigned v) { return __hip_atomic_fetch_add(p, v, __ATOMIC_RELAXED, __HIP_MEMORY_SCOPE_AGENT); }
; #define XB_SPIN(cond, bar) do { unsigned _sp = 0; while (cond) { __builtin_amdgcn_s_sleep(1); \
;     if ((++_sp & 255u) == 0u) { if (xb_ld(&(bar)[XB_TMO])) break; if (_sp > XB_SPIN_CAP) { atomicAdd(&(bar)[XB_TMO], 1u); break; } } } } while (0)
; __device__ __forceinline__ void xcd_barrier(const XcdBarrier& b) {
;     ...
;         const unsigned old = xb_add(&bar[XB_XSUB(b.x)], 1u);
;         const unsigned gen = old / nloc;
;         if (old + 1u == (gen + 1u) * nloc) {
;             __builtin_amdgcn_fence(__ATOMIC_RELEASE, "agent");
;             asm volatile("s_waitcnt vmcnt(0)" ::: "memory");
;             const unsigned og = xb_add(&bar[XB_TOP], 1u);
;             const unsigned tg = og / nx;
;             if (og + 1u == (tg + 1u) * nx) xb_add(&bar[XB_TOPGEN], 1u);
;             else XB_SPIN(xb_ld(&bar[XB_TOPGEN]) == tg, bar);
;             __builtin_amdgcn_fence(__ATOMIC_ACQUIRE, "agent");
;             xb_add(&bar[XB_XGEN(b.x)], 1u);
;             asm volatile("s_waitcnt vmcnt(0)" ::: "memory");
;         } else {
;             XB_SPIN(xb_ld(&bar[XB_XGEN(b.x)]) == gen, bar);
.LBB0_122:
	s_mov_b64 s[10:11], exec
	s_lshl_b32 s8, s33, 8
	v_readlane_b32 s0, v252, 2
	v_mbcnt_lo_u32_b32 v2, s10, 0
	v_readlane_b32 s1, v252, 3
	s_add_u32 s8, s0, s8
	v_mbcnt_hi_u32_b32 v2, s11, v2
	s_addc_u32 s9, s1, 0
	v_cmp_eq_u32_e32 vcc, 0, v2
	s_and_saveexec_b64 s[28:29], vcc
	s_cbranch_execz .LBB0_124
	s_bcnt1_i32_b64 s10, s[10:11]
	v_mov_b32_e32 v4, 0x1000
	v_mov_b32_e32 v5, s10
	global_atomic_add v4, v4, v5, s[8:9] offset:1024 sc0
	buffer_inv sc1
.LBB0_124:
	s_or_b64 exec, exec, s[28:29]
	v_cvt_f32_u32_e32 v5, v3
	s_waitcnt vmcnt(1)
	v_readfirstlane_b32 s10, v4
	v_sub_u32_e32 v4, 0, v3
	v_rcp_iflag_f32_e32 v5, v5
	v_add_u32_e32 v6, s10, v2
	v_mul_f32_e32 v5, 0x4f7ffffe, v5
	v_cvt_u32_f32_e32 v5, v5
	v_mul_lo_u32 v2, v4, v5
	v_mul_hi_u32 v2, v5, v2
	v_add_u32_e32 v2, v5, v2
	v_mul_hi_u32 v2, v6, v2
	v_mul_lo_u32 v4, v2, v3
	v_sub_u32_e32 v4, v6, v4
	v_add_u32_e32 v5, 1, v2
	v_cmp_ge_u32_e32 vcc, v4, v3
	s_nop 1
	v_cndmask_b32_e32 v2, v2, v5, vcc
	v_sub_u32_e32 v5, v4, v3
	v_cndmask_b32_e32 v4, v4, v5, vcc
	v_add_u32_e32 v5, 1, v2
	v_cmp_ge_u32_e32 vcc, v4, v3
	v_add_u32_e32 v4, 1, v6
	s_nop 0
	v_cndmask_b32_e32 v2, v2, v5, vcc
	v_mul_lo_u32 v5, v3, v2
	v_add_u32_e32 v3, v5, v3
	v_cmp_ne_u32_e32 vcc, v4, v3
	s_and_saveexec_b64 s[10:11], vcc
	s_xor_b64 s[10:11], exec, s[10:11]
	s_cbranch_execz .LBB0_138
	s_waitcnt lgkmcnt(0)
	v_mov_b32_e32 v1, 0x2000
	global_load_dword v1, v1, s[8:9] offset:1024 sc1
	s_add_u32 s34, s8, 0x2400
	s_addc_u32 s35, s9, 0
	s_waitcnt vmcnt(0)
	v_cmp_eq_u32_e32 vcc, v1, v2
	s_and_saveexec_b64 s[28:29], vcc
	s_cbranch_execz .LBB0_137
	s_add_u32 s30, s22, 0x4200
	s_addc_u32 s31, s23, 0
	s_mov_b32 s14, 1
	s_mov_b64 s[36:37], 0
	v_mov_b32_e32 v1, 0
	s_branch .LBB0_128

; __device__ __forceinline__ unsigned xb_ld(unsigned* p)              { return __hip_atomic_load(p, __ATOMIC_RELAXED, __HIP_MEMORY_SCOPE_AGENT); }
; #define XB_SPIN(cond, bar) do { unsigned _sp = 0; while (cond) { __builtin_amdgcn_s_sleep(1); \
;     if ((++_sp & 255u) == 0u) { if (xb_ld(&(bar)[XB_TMO])) break; if (_sp > XB_SPIN_CAP) { atomicAdd(&(bar)[XB_TMO], 1u); break; } } } } while (0)
; __device__ __forceinline__ void xcd_barrier(const XcdBarrier& b) {
;     ...
;             XB_SPIN(xb_ld(&bar[XB_XGEN(b.x)]) == gen, bar);
;             __builtin_amdgcn_fence(__ATOMIC_ACQUIRE, "agent");
;             asm volatile("s_waitcnt vmcnt(0)" ::: "memory");
.LBB0_137:
	s_or_b64 exec, exec, s[28:29]
	s_waitcnt vmcnt(0)
	s_waitcnt vmcnt(0)

; __device__ __forceinline__ unsigned xb_ld(unsigned* p)              { return __hip_atomic_load(p, __ATOMIC_RELAXED, __HIP_MEMORY_SCOPE_AGENT); }
; __device__ __forceinline__ unsigned xb_add(unsigned* p, unsigned v) { return __hip_atomic_fetch_add(p, v, __ATOMIC_RELAXED, __HIP_MEMORY_SCOPE_AGENT); }
; #define XB_SPIN(cond, bar) do { unsigned _sp = 0; while (cond) { __builtin_amdgcn_s_sleep(1); \
;     if ((++_sp & 255u) == 0u) { if (xb_ld(&(bar)[XB_TMO])) break; if (_sp > XB_SPIN_CAP) { atomicAdd(&(bar)[XB_TMO], 1u); break; } } } } while (0)
; __device__ __forceinline__ void xcd_barrier(const XcdBarrier& b) {
;     ...
;             else XB_SPIN(xb_ld(&bar[XB_TOPGEN]) == tg, bar);
;             __builtin_amdgcn_fence(__ATOMIC_ACQUIRE, "agent");
;             xb_add(&bar[XB_XGEN(b.x)], 1u);
;             asm volatile("s_waitcnt vmcnt(0)" ::: "memory");
.LBB0_155:
	s_or_b64 exec, exec, s[10:11]
	s_mov_b64 s[10:11], exec
	v_mbcnt_lo_u32_b32 v1, s10, 0
	v_mbcnt_hi_u32_b32 v1, s11, v1
	v_cmp_eq_u32_e32 vcc, 0, v1
	s_waitcnt vmcnt(0)
	s_and_saveexec_b64 s[28:29], vcc
	s_cbranch_execz .LBB0_157
	s_bcnt1_i32_b64 s10, s[10:11]
	v_mov_b32_e32 v1, 0x2000
	v_mov_b32_e32 v2, s10
	global_atomic_add v1, v2, s[8:9] offset:1024

; __device__ __forceinline__ unsigned xb_ld(unsigned* p)              { return __hip_atomic_load(p, __ATOMIC_RELAXED, __HIP_MEMORY_SCOPE_AGENT); }
; __device__ __forceinline__ unsigned xb_add(unsigned* p, unsigned v) { return __hip_atomic_fetch_add(p, v, __ATOMIC_RELAXED, __HIP_MEMORY_SCOPE_AGENT); }
; #define XB_SPIN(cond, bar) do { unsigned _sp = 0; while (cond) { __builtin_amdgcn_s_sleep(1); \
;     if ((++_sp & 255u) == 0u) { if (xb_ld(&(bar)[XB_TMO])) break; if (_sp > XB_SPIN_CAP) { atomicAdd(&(bar)[XB_TMO], 1u); break; } } } } while (0)
; __device__ __forceinline__ void xcd_barrier(const XcdBarrier& b) {
;     ...
;         const unsigned old = xb_add(&bar[XB_XSUB(b.x)], 1u);
;         const unsigned gen = old / nloc;
;         if (old + 1u == (gen + 1u) * nloc) {
;             __builtin_amdgcn_fence(__ATOMIC_RELEASE, "agent");
;             asm volatile("s_waitcnt vmcnt(0)" ::: "memory");
;             const unsigned og = xb_add(&bar[XB_TOP], 1u);
;             const unsigned tg = og / nx;
;             if (og + 1u == (tg + 1u) * nx) xb_add(&bar[XB_TOPGEN], 1u);
;             else XB_SPIN(xb_ld(&bar[XB_TOPGEN]) == tg, bar);
;             __builtin_amdgcn_fence(__ATOMIC_ACQUIRE, "agent");
;             xb_add(&bar[XB_XGEN(b.x)], 1u);
;             asm volatile("s_waitcnt vmcnt(0)" ::: "memory");
;         } else {
;             XB_SPIN(xb_ld(&bar[XB_XGEN(b.x)]) == gen, bar);
.LBB0_904:
	s_mov_b64 s[8:9], exec
	v_readlane_b32 s0, v252, 12
	s_lshl_b32 s6, s0, 8
	v_readlane_b32 s0, v252, 8
	v_mbcnt_lo_u32_b32 v2, s8, 0
	v_readlane_b32 s1, v252, 9
	s_add_u32 s6, s0, s6
	v_mbcnt_hi_u32_b32 v2, s9, v2
	s_addc_u32 s7, s1, 0
	v_cmp_eq_u32_e32 vcc, 0, v2
	s_and_saveexec_b64 s[10:11], vcc
	s_cbranch_execz .LBB0_906
	s_bcnt1_i32_b64 s8, s[8:9]
	v_mov_b32_e32 v4, 0x1000
	v_mov_b32_e32 v5, s8
	global_atomic_add v4, v4, v5, s[6:7] offset:1024 sc0
	buffer_inv sc1
.LBB0_906:
	s_or_b64 exec, exec, s[10:11]
	v_cvt_f32_u32_e32 v5, v3
	s_waitcnt vmcnt(1)
	v_readfirstlane_b32 s8, v4
	v_sub_u32_e32 v4, 0, v3
	v_rcp_iflag_f32_e32 v5, v5
	v_add_u32_e32 v6, s8, v2
	v_mul_f32_e32 v5, 0x4f7ffffe, v5
	v_cvt_u32_f32_e32 v5, v5
	v_mul_lo_u32 v2, v4, v5
	v_mul_hi_u32 v2, v5, v2
	v_add_u32_e32 v2, v5, v2
	v_mul_hi_u32 v2, v6, v2
	v_mul_lo_u32 v4, v2, v3
	v_sub_u32_e32 v4, v6, v4
	v_add_u32_e32 v5, 1, v2
	v_cmp_ge_u32_e32 vcc, v4, v3
	s_nop 1
	v_cndmask_b32_e32 v2, v2, v5, vcc
	v_sub_u32_e32 v5, v4, v3
	v_cndmask_b32_e32 v4, v4, v5, vcc
	v_add_u32_e32 v5, 1, v2
	v_cmp_ge_u32_e32 vcc, v4, v3
	v_add_u32_e32 v4, 1, v6
	s_nop 0
	v_cndmask_b32_e32 v2, v2, v5, vcc
	v_mul_lo_u32 v5, v3, v2
	v_add_u32_e32 v3, v5, v3
	v_cmp_ne_u32_e32 vcc, v4, v3
	s_and_saveexec_b64 s[8:9], vcc
	s_xor_b64 s[8:9], exec, s[8:9]
	s_cbranch_execz .LBB0_920
	s_waitcnt lgkmcnt(0)
	v_mov_b32_e32 v1, 0x2000
	global_load_dword v1, v1, s[6:7] offset:1024 sc1
	s_add_u32 s16, s6, 0x2400
	s_addc_u32 s17, s7, 0
	s_waitcnt vmcnt(0)
	v_cmp_eq_u32_e32 vcc, v1, v2
	s_and_saveexec_b64 s[10:11], vcc
	s_cbranch_execz .LBB0_919
	s_add_u32 s12, s22, 0xc200
	s_addc_u32 s13, s23, 0
	s_mov_b32 s14, 1
	s_mov_b64 s[28:29], 0
	v_mov_b32_e32 v1, 0
	s_branch .LBB0_910

; __device__ __forceinline__ unsigned xb_ld(unsigned* p)              { return __hip_atomic_load(p, __ATOMIC_RELAXED, __HIP_MEMORY_SCOPE_AGENT); }
; #define XB_SPIN(cond, bar) do { unsigned _sp = 0; while (cond) { __builtin_amdgcn_s_sleep(1); \
;     if ((++_sp & 255u) == 0u) { if (xb_ld(&(bar)[XB_TMO])) break; if (_sp > XB_SPIN_CAP) { atomicAdd(&(bar)[XB_TMO], 1u); break; } } } } while (0)
; __device__ __forceinline__ void xcd_barrier(const XcdBarrier& b) {
;     ...
;             XB_SPIN(xb_ld(&bar[XB_XGEN(b.x)]) == gen, bar);
;             __builtin_amdgcn_fence(__ATOMIC_ACQUIRE, "agent");
;             asm volatile("s_waitcnt vmcnt(0)" ::: "memory");
.LBB0_919:
	s_or_b64 exec, exec, s[10:11]
	s_waitcnt vmcnt(0)
	s_waitcnt vmcnt(0)

; __device__ __forceinline__ unsigned xb_ld(unsigned* p)              { return __hip_atomic_load(p, __ATOMIC_RELAXED, __HIP_MEMORY_SCOPE_AGENT); }
; __device__ __forceinline__ unsigned xb_add(unsigned* p, unsigned v) { return __hip_atomic_fetch_add(p, v, __ATOMIC_RELAXED, __HIP_MEMORY_SCOPE_AGENT); }
; #define XB_SPIN(cond, bar) do { unsigned _sp = 0; while (cond) { __builtin_amdgcn_s_sleep(1); \
;     if ((++_sp & 255u) == 0u) { if (xb_ld(&(bar)[XB_TMO])) break; if (_sp > XB_SPIN_CAP) { atomicAdd(&(bar)[XB_TMO], 1u); break; } } } } while (0)
; __device__ __forceinline__ void xcd_barrier(const XcdBarrier& b) {
;     ...
;         const unsigned old = xb_add(&bar[XB_XSUB(b.x)], 1u);
;         const unsigned gen = old / nloc;
;         if (old + 1u == (gen + 1u) * nloc) {
;             __builtin_amdgcn_fence(__ATOMIC_RELEASE, "agent");
;             asm volatile("s_waitcnt vmcnt(0)" ::: "memory");
;             const unsigned og = xb_add(&bar[XB_TOP], 1u);
;             const unsigned tg = og / nx;
;             if (og + 1u == (tg + 1u) * nx) xb_add(&bar[XB_TOPGEN], 1u);
;             else XB_SPIN(xb_ld(&bar[XB_TOPGEN]) == tg, bar);
;             __builtin_amdgcn_fence(__ATOMIC_ACQUIRE, "agent");
;             xb_add(&bar[XB_XGEN(b.x)], 1u);
;             asm volatile("s_waitcnt vmcnt(0)" ::: "memory");
;         } else {
;             XB_SPIN(xb_ld(&bar[XB_XGEN(b.x)]) == gen, bar);
.LBB0_938:
	s_mov_b64 s[10:11], exec
	s_lshl_b32 s8, s33, 8
	v_readlane_b32 s0, v252, 2
	v_mbcnt_lo_u32_b32 v2, s10, 0
	v_readlane_b32 s1, v252, 3
	s_add_u32 s8, s0, s8
	v_mbcnt_hi_u32_b32 v2, s11, v2
	s_addc_u32 s9, s1, 0
	v_cmp_eq_u32_e32 vcc, 0, v2
	s_and_saveexec_b64 s[12:13], vcc
	s_cbranch_execz .LBB0_940
	s_bcnt1_i32_b64 s10, s[10:11]
	v_mov_b32_e32 v4, 0x1000
	v_mov_b32_e32 v5, s10
	global_atomic_add v4, v4, v5, s[8:9] offset:1024 sc0
	buffer_inv sc1
.LBB0_940:
	s_or_b64 exec, exec, s[12:13]
	v_cvt_f32_u32_e32 v5, v3
	s_waitcnt vmcnt(1)
	v_readfirstlane_b32 s10, v4
	v_sub_u32_e32 v4, 0, v3
	v_rcp_iflag_f32_e32 v5, v5
	v_add_u32_e32 v6, s10, v2
	v_mul_f32_e32 v5, 0x4f7ffffe, v5
	v_cvt_u32_f32_e32 v5, v5
	v_mul_lo_u32 v2, v4, v5
	v_mul_hi_u32 v2, v5, v2
	v_add_u32_e32 v2, v5, v2
	v_mul_hi_u32 v2, v6, v2
	v_mul_lo_u32 v4, v2, v3
	v_sub_u32_e32 v4, v6, v4
	v_add_u32_e32 v5, 1, v2
	v_cmp_ge_u32_e32 vcc, v4, v3
	s_nop 1
	v_cndmask_b32_e32 v2, v2, v5, vcc
	v_sub_u32_e32 v5, v4, v3
	v_cndmask_b32_e32 v4, v4, v5, vcc
	v_add_u32_e32 v5, 1, v2
	v_cmp_ge_u32_e32 vcc, v4, v3
	v_add_u32_e32 v4, 1, v6
	s_nop 0
	v_cndmask_b32_e32 v2, v2, v5, vcc
	v_mul_lo_u32 v5, v3, v2
	v_add_u32_e32 v3, v5, v3
	v_cmp_ne_u32_e32 vcc, v4, v3
	s_and_saveexec_b64 s[10:11], vcc
	s_xor_b64 s[10:11], exec, s[10:11]
	s_cbranch_execz .LBB0_1585
	s_waitcnt lgkmcnt(0)
	v_mov_b32_e32 v1, 0x2000
	global_load_dword v1, v1, s[8:9] offset:1024 sc1
	s_add_u32 s30, s8, 0x2400
	s_addc_u32 s31, s9, 0
	s_waitcnt vmcnt(0)
	v_cmp_eq_u32_e32 vcc, v1, v2
	s_and_saveexec_b64 s[12:13], vcc
	s_cbranch_execz .LBB0_1584
	s_add_u32 s28, s22, 0x4200
	s_addc_u32 s29, s23, 0
	s_mov_b32 s14, 1
	s_mov_b64 s[34:35], 0
	v_mov_b32_e32 v1, 0
	s_branch .LBB0_944

; __device__ __forceinline__ unsigned xb_ld(unsigned* p)              { return __hip_atomic_load(p, __ATOMIC_RELAXED, __HIP_MEMORY_SCOPE_AGENT); }
; __device__ __forceinline__ unsigned xb_add(unsigned* p, unsigned v) { return __hip_atomic_fetch_add(p, v, __ATOMIC_RELAXED, __HIP_MEMORY_SCOPE_AGENT); }
; #define XB_SPIN(cond, bar) do { unsigned _sp = 0; while (cond) { __builtin_amdgcn_s_sleep(1); \
;     if ((++_sp & 255u) == 0u) { if (xb_ld(&(bar)[XB_TMO])) break; if (_sp > XB_SPIN_CAP) { atomicAdd(&(bar)[XB_TMO], 1u); break; } } } } while (0)
; __device__ __forceinline__ void xcd_barrier(const XcdBarrier& b) {
;     ...
;             else XB_SPIN(xb_ld(&bar[XB_TOPGEN]) == tg, bar);
;             __builtin_amdgcn_fence(__ATOMIC_ACQUIRE, "agent");
;             xb_add(&bar[XB_XGEN(b.x)], 1u);
;             asm volatile("s_waitcnt vmcnt(0)" ::: "memory");
.LBB0_954:
	s_or_b64 exec, exec, s[8:9]
	s_mov_b64 s[8:9], exec
	v_mbcnt_lo_u32_b32 v1, s8, 0
	v_mbcnt_hi_u32_b32 v1, s9, v1
	v_cmp_eq_u32_e32 vcc, 0, v1
	s_waitcnt vmcnt(0)
	s_and_saveexec_b64 s[10:11], vcc
	s_cbranch_execz .LBB0_956
	s_bcnt1_i32_b64 s8, s[8:9]
	v_mov_b32_e32 v1, 0x2000
	v_mov_b32_e32 v2, s8
	global_atomic_add v1, v2, s[6:7] offset:1024

; __device__ __forceinline__ unsigned xb_ld(unsigned* p)              { return __hip_atomic_load(p, __ATOMIC_RELAXED, __HIP_MEMORY_SCOPE_AGENT); }
; __device__ __forceinline__ unsigned xb_add(unsigned* p, unsigned v) { return __hip_atomic_fetch_add(p, v, __ATOMIC_RELAXED, __HIP_MEMORY_SCOPE_AGENT); }
; #define XB_SPIN(cond, bar) do { unsigned _sp = 0; while (cond) { __builtin_amdgcn_s_sleep(1); \
;     if ((++_sp & 255u) == 0u) { if (xb_ld(&(bar)[XB_TMO])) break; if (_sp > XB_SPIN_CAP) { atomicAdd(&(bar)[XB_TMO], 1u); break; } } } } while (0)
; __device__ __forceinline__ void xcd_barrier(const XcdBarrier& b) {
;     ...
;         const unsigned gen = old / nloc;
;         if (old + 1u == (gen + 1u) * nloc) {
;             __builtin_amdgcn_fence(__ATOMIC_RELEASE, "agent");
;             asm volatile("s_waitcnt vmcnt(0)" ::: "memory");
;             const unsigned og = xb_add(&bar[XB_TOP], 1u);
;             const unsigned tg = og / nx;
;             if (og + 1u == (tg + 1u) * nx) xb_add(&bar[XB_TOPGEN], 1u);
;             else XB_SPIN(xb_ld(&bar[XB_TOPGEN]) == tg, bar);
;             __builtin_amdgcn_fence(__ATOMIC_ACQUIRE, "agent");
;             xb_add(&bar[XB_XGEN(b.x)], 1u);
;             asm volatile("s_waitcnt vmcnt(0)" ::: "memory");
;         } else {
;             XB_SPIN(xb_ld(&bar[XB_XGEN(b.x)]) == gen, bar);
.LBB0_1043:
	s_or_b64 exec, exec, s[12:13]
	v_cvt_f32_u32_e32 v5, v3
	s_waitcnt vmcnt(1)
	v_readfirstlane_b32 s10, v4
	v_sub_u32_e32 v4, 0, v3
	v_rcp_iflag_f32_e32 v5, v5
	v_add_u32_e32 v6, s10, v2
	v_mul_f32_e32 v5, 0x4f7ffffe, v5
	v_cvt_u32_f32_e32 v5, v5
	v_mul_lo_u32 v2, v4, v5
	v_mul_hi_u32 v2, v5, v2
	v_add_u32_e32 v2, v5, v2
	v_mul_hi_u32 v2, v6, v2
	v_mul_lo_u32 v4, v2, v3
	v_sub_u32_e32 v4, v6, v4
	v_add_u32_e32 v5, 1, v2
	v_cmp_ge_u32_e32 vcc, v4, v3
	s_nop 1
	v_cndmask_b32_e32 v2, v2, v5, vcc
	v_sub_u32_e32 v5, v4, v3
	v_cndmask_b32_e32 v4, v4, v5, vcc
	v_add_u32_e32 v5, 1, v2
	v_cmp_ge_u32_e32 vcc, v4, v3
	v_add_u32_e32 v4, 1, v6
	s_nop 0
	v_cndmask_b32_e32 v2, v2, v5, vcc
	v_mul_lo_u32 v5, v3, v2
	v_add_u32_e32 v3, v5, v3
	v_cmp_ne_u32_e32 vcc, v4, v3
	s_and_saveexec_b64 s[10:11], vcc
	s_xor_b64 s[10:11], exec, s[10:11]
	s_cbranch_execz .LBB0_1057
	s_waitcnt lgkmcnt(0)
	v_mov_b32_e32 v1, 0x2000
	global_load_dword v1, v1, s[8:9] offset:1024 sc1
	s_add_u32 s16, s8, 0x2400
	s_addc_u32 s17, s9, 0
	s_waitcnt vmcnt(0)
	v_cmp_eq_u32_e32 vcc, v1, v2
	s_and_saveexec_b64 s[12:13], vcc
	s_cbranch_execz .LBB0_1056
	s_add_u32 s14, s22, 0x4200
	s_addc_u32 s15, s23, 0
	s_mov_b32 s18, 1
	s_mov_b64 s[28:29], 0
	v_mov_b32_e32 v1, 0
	s_branch .LBB0_1047

; __device__ __forceinline__ unsigned xb_ld(unsigned* p)              { return __hip_atomic_load(p, __ATOMIC_RELAXED, __HIP_MEMORY_SCOPE_AGENT); }
; #define XB_SPIN(cond, bar) do { unsigned _sp = 0; while (cond) { __builtin_amdgcn_s_sleep(1); \
;     if ((++_sp & 255u) == 0u) { if (xb_ld(&(bar)[XB_TMO])) break; if (_sp > XB_SPIN_CAP) { atomicAdd(&(bar)[XB_TMO], 1u); break; } } } } while (0)
; __device__ __forceinline__ void xcd_barrier(const XcdBarrier& b) {
;     ...
;             XB_SPIN(xb_ld(&bar[XB_XGEN(b.x)]) == gen, bar);
;             __builtin_amdgcn_fence(__ATOMIC_ACQUIRE, "agent");
;             asm volatile("s_waitcnt vmcnt(0)" ::: "memory");
.LBB0_1056:
	s_or_b64 exec, exec, s[12:13]
	s_waitcnt vmcnt(0)
	s_waitcnt vmcnt(0)

; __device__ __forceinline__ unsigned xb_ld(unsigned* p)              { return __hip_atomic_load(p, __ATOMIC_RELAXED, __HIP_MEMORY_SCOPE_AGENT); }
; __device__ __forceinline__ unsigned xb_add(unsigned* p, unsigned v) { return __hip_atomic_fetch_add(p, v, __ATOMIC_RELAXED, __HIP_MEMORY_SCOPE_AGENT); }
; #define XB_SPIN(cond, bar) do { unsigned _sp = 0; while (cond) { __builtin_amdgcn_s_sleep(1); \
;     if ((++_sp & 255u) == 0u) { if (xb_ld(&(bar)[XB_TMO])) break; if (_sp > XB_SPIN_CAP) { atomicAdd(&(bar)[XB_TMO], 1u); break; } } } } while (0)
; __device__ __forceinline__ void xcd_barrier(const XcdBarrier& b) {
;     ...
;             else XB_SPIN(xb_ld(&bar[XB_TOPGEN]) == tg, bar);
;             __builtin_amdgcn_fence(__ATOMIC_ACQUIRE, "agent");
;             xb_add(&bar[XB_XGEN(b.x)], 1u);
;             asm volatile("s_waitcnt vmcnt(0)" ::: "memory");
.LBB0_1074:
	s_or_b64 exec, exec, s[10:11]
	s_mov_b64 s[10:11], exec
	v_mbcnt_lo_u32_b32 v1, s10, 0
	v_mbcnt_hi_u32_b32 v1, s11, v1
	v_cmp_eq_u32_e32 vcc, 0, v1
	s_waitcnt vmcnt(0)
	s_and_saveexec_b64 s[12:13], vcc
	s_cbranch_execz .LBB0_1076
	s_bcnt1_i32_b64 s10, s[10:11]
	v_mov_b32_e32 v1, 0x2000
	v_mov_b32_e32 v2, s10
	global_atomic_add v1, v2, s[8:9] offset:1024

; __device__ __forceinline__ unsigned xb_ld(unsigned* p)              { return __hip_atomic_load(p, __ATOMIC_RELAXED, __HIP_MEMORY_SCOPE_AGENT); }
; __device__ __forceinline__ unsigned xb_add(unsigned* p, unsigned v) { return __hip_atomic_fetch_add(p, v, __ATOMIC_RELAXED, __HIP_MEMORY_SCOPE_AGENT); }
; #define XB_SPIN(cond, bar) do { unsigned _sp = 0; while (cond) { __builtin_amdgcn_s_sleep(1); \
;     if ((++_sp & 255u) == 0u) { if (xb_ld(&(bar)[XB_TMO])) break; if (_sp > XB_SPIN_CAP) { atomicAdd(&(bar)[XB_TMO], 1u); break; } } } } while (0)
; __device__ __forceinline__ void xcd_barrier(const XcdBarrier& b) {
;     ...
;         const unsigned old = xb_add(&bar[XB_XSUB(b.x)], 1u);
;         const unsigned gen = old / nloc;
;         if (old + 1u == (gen + 1u) * nloc) {
;             __builtin_amdgcn_fence(__ATOMIC_RELEASE, "agent");
;             asm volatile("s_waitcnt vmcnt(0)" ::: "memory");
;             const unsigned og = xb_add(&bar[XB_TOP], 1u);
;             const unsigned tg = og / nx;
;             if (og + 1u == (tg + 1u) * nx) xb_add(&bar[XB_TOPGEN], 1u);
;             else XB_SPIN(xb_ld(&bar[XB_TOPGEN]) == tg, bar);
;             __builtin_amdgcn_fence(__ATOMIC_ACQUIRE, "agent");
;             xb_add(&bar[XB_XGEN(b.x)], 1u);
;             asm volatile("s_waitcnt vmcnt(0)" ::: "memory");
;         } else {
;             XB_SPIN(xb_ld(&bar[XB_XGEN(b.x)]) == gen, bar);
.LBB0_1539:
	s_mov_b64 s[10:11], exec
	s_lshl_b32 s1, s33, 8
	v_readlane_b32 s8, v252, 2
	v_mbcnt_lo_u32_b32 v2, s10, 0
	v_readlane_b32 s9, v252, 3
	s_add_u32 s8, s8, s1
	v_mbcnt_hi_u32_b32 v2, s11, v2
	s_addc_u32 s9, s9, 0
	v_cmp_eq_u32_e32 vcc, 0, v2
	s_and_saveexec_b64 s[12:13], vcc
	s_cbranch_execz .LBB0_1541
	s_bcnt1_i32_b64 s1, s[10:11]
	v_mov_b32_e32 v4, 0x1000
	v_mov_b32_e32 v5, s1
	global_atomic_add v4, v4, v5, s[8:9] offset:1024 sc0
	buffer_inv sc1
.LBB0_1541:
	s_or_b64 exec, exec, s[12:13]
	v_cvt_f32_u32_e32 v5, v3
	s_waitcnt vmcnt(1)
	v_readfirstlane_b32 s1, v4
	v_sub_u32_e32 v4, 0, v3
	v_rcp_iflag_f32_e32 v5, v5
	v_add_u32_e32 v6, s1, v2
	v_mul_f32_e32 v5, 0x4f7ffffe, v5
	v_cvt_u32_f32_e32 v5, v5
	v_mul_lo_u32 v2, v4, v5
	v_mul_hi_u32 v2, v5, v2
	v_add_u32_e32 v2, v5, v2
	v_mul_hi_u32 v2, v6, v2
	v_mul_lo_u32 v4, v2, v3
	v_sub_u32_e32 v4, v6, v4
	v_add_u32_e32 v5, 1, v2
	v_cmp_ge_u32_e32 vcc, v4, v3
	s_nop 1
	v_cndmask_b32_e32 v2, v2, v5, vcc
	v_sub_u32_e32 v5, v4, v3
	v_cndmask_b32_e32 v4, v4, v5, vcc
	v_add_u32_e32 v5, 1, v2
	v_cmp_ge_u32_e32 vcc, v4, v3
	v_add_u32_e32 v4, 1, v6
	s_nop 0
	v_cndmask_b32_e32 v2, v2, v5, vcc
	v_mul_lo_u32 v5, v3, v2
	v_add_u32_e32 v3, v5, v3
	v_cmp_ne_u32_e32 vcc, v4, v3
	s_and_saveexec_b64 s[10:11], vcc
	s_xor_b64 s[10:11], exec, s[10:11]
	s_cbranch_execz .LBB0_1555
	s_waitcnt lgkmcnt(0)
	v_mov_b32_e32 v1, 0x2000
	global_load_dword v1, v1, s[8:9] offset:1024 sc1
	s_add_u32 s16, s8, 0x2400
	s_addc_u32 s17, s9, 0
	s_waitcnt vmcnt(0)
	v_cmp_eq_u32_e32 vcc, v1, v2
	s_and_saveexec_b64 s[12:13], vcc
	s_cbranch_execz .LBB0_1554
	s_add_u32 s14, s22, 0x4200
	s_addc_u32 s15, s23, 0
	s_mov_b32 s1, 1
	s_mov_b64 s[18:19], 0
	v_mov_b32_e32 v1, 0
	s_branch .LBB0_1545

; __device__ __forceinline__ unsigned xb_ld(unsigned* p)              { return __hip_atomic_load(p, __ATOMIC_RELAXED, __HIP_MEMORY_SCOPE_AGENT); }
; __device__ __forceinline__ unsigned xb_add(unsigned* p, unsigned v) { return __hip_atomic_fetch_add(p, v, __ATOMIC_RELAXED, __HIP_MEMORY_SCOPE_AGENT); }
; #define XB_SPIN(cond, bar) do { unsigned _sp = 0; while (cond) { __builtin_amdgcn_s_sleep(1); \
;     if ((++_sp & 255u) == 0u) { if (xb_ld(&(bar)[XB_TMO])) break; if (_sp > XB_SPIN_CAP) { atomicAdd(&(bar)[XB_TMO], 1u); break; } } } } while (0)
; __device__ __forceinline__ void xcd_barrier(const XcdBarrier& b) {
;     ...
;             else XB_SPIN(xb_ld(&bar[XB_TOPGEN]) == tg, bar);
;             __builtin_amdgcn_fence(__ATOMIC_ACQUIRE, "agent");
;             xb_add(&bar[XB_XGEN(b.x)], 1u);
;             asm volatile("s_waitcnt vmcnt(0)" ::: "memory");
.LBB0_1572:
	s_or_b64 exec, exec, s[10:11]
	s_mov_b64 s[10:11], exec
	v_mbcnt_lo_u32_b32 v1, s10, 0
	v_mbcnt_hi_u32_b32 v1, s11, v1
	v_cmp_eq_u32_e32 vcc, 0, v1
	s_waitcnt vmcnt(0)
	s_and_saveexec_b64 s[12:13], vcc
	s_cbranch_execz .LBB0_1574
	s_bcnt1_i32_b64 s1, s[10:11]
	v_mov_b32_e32 v1, 0x2000
	v_mov_b32_e32 v2, s1
	global_atomic_add v1, v2, s[8:9] offset:1024
